# speedup vs baseline: 1.0015x; 1.0015x over previous
.LBB0_20:
	s_or_b64 exec, exec, s[16:17]
	s_waitcnt vmcnt(0)
	v_add_f32_e32 v21, v2, v3
	v_mov_b32_e32 v86, v21

.LBB0_35:
	s_or_b64 exec, exec, s[18:19]
	s_waitcnt vmcnt(0)
	v_add_f32_e32 v18, v2, v3
	v_mov_b32_e32 v87, v18

.LBB0_44:
	s_or_b64 exec, exec, s[16:17]
	v_or_b32_e32 v14, 16, v8
	s_and_saveexec_b64 s[16:17], s[2:3]
	s_cbranch_execz .LBB0_57
	s_and_b64 vcc, exec, s[0:1]
	v_mov_b32_e32 v15, 0
	s_cbranch_vccnz .LBB0_49
	v_mov_b32_e32 v15, v86

.LBB0_61:
	v_mov_b32_e32 v2, v87
